# pass-B cache warming by four idle waves in the second layer (one wave where the others copy weights)
# baseline (speedup 1.0000x reference)
; #define IN(k) (((PHMASK >> PHBIT(k)) & 1u) && lo <= (k) && (k) < hi)
; #define DUP(bit) if constexpr (((PROBE_DUP >> (bit)) & 1u) != 0u)
; DI void phase_chunkB(const Args& a, LAS unsigned char* lds, int wave, int lane, int bid, int G) {
;     ...
;     for (int u = bid; u < NB * NH * 4; u += G) { const int iq = u & 3, bh = u >> 2;
;         bf16x8 pf[3][4][2]; f32x4 qv[3][4];
; __global__ void __launch_bounds__(NTHR, 2) mk_fwd(ArgsV argsv) {
;     ...
;         if (IN(pb + 3)) { { PH_BEGIN(); phase_chunkA(a, lds, wave, lane, tid, bid, G); } DUP(PB_CKA) { PH_BEGIN(); phase_chunkA(a, lds, wave, lane, tid, bid, G); }
;             { PH_BEGIN(); phase_attn(a, l, gw, NGW, lane); } DUP(PB_ATTN) { PH_BEGIN(); phase_attn(a, l, gw, NGW, lane); }
;             xcd_barrier(bar);
;             { PH_BEGIN(); phase_chunkB(a, lds, wave, lane, bid, G); if (wave != 0 && wave != 4 && l == 0) phase_convert<1>(a, 0, lds, bid * (NWAVES - 2) + (wave < 4 ? wave - 1 : wave - 2), G * (NWAVES - 2), wave, lane); }
;             DUP(PB_CKB) { PH_BEGIN(); phase_chunkB(a, lds, wave, lane, bid, G); } xcd_barrier(bar);
.LBB0_1158:
	s_lshr_b32 s3, s2, 6
	s_cmp_lt_u32 s3, 4
	s_cbranch_scc1 .Lcbh_skip
	s_sub_i32 s4, s3, 4
	s_mov_b32 s5, 1
	s_mov_b32 s29, 32
	v_readlane_b32 s24, v254, 1
	s_cmp_lg_u32 s24, 0
	s_cbranch_scc1 .Lcbh_l0
	s_mov_b32 s5, 4
	s_mov_b32 s29, 8
	s_branch .Lcbh_go
.Lcbh_l0:
	s_cmp_lg_u32 s4, 0
	s_cbranch_scc1 .Lcbh_skip
.Lcbh_go:
	s_lshl_b32 s24, s4, 13
	s_lshl_b32 s25, s4, 14
	s_lshl_b32 s36, s5, 13
	s_lshl_b32 s37, s5, 14
	v_and_b32_e32 v8, 63, v0
	v_lshlrev_b32_e32 v9, 4, v8
	v_add_u32_e32 v10, 0x1000, v9
	v_lshrrev_b32_e32 v11, 2, v8
	v_and_b32_e32 v12, 3, v8
	v_lshlrev_b32_e32 v12, 4, v12
	v_lshl_or_b32 v11, v11, 8, v12
	v_add_u32_e32 v12, 0x1000, v11
	v_add_u32_e32 v13, 0x2000, v11
	v_add_u32_e32 v50, 0x3000, v11
	s_mov_b32 s28, s1
.Lcbh_unit:
	s_cmpk_gt_i32 s28, 0xff
	s_cbranch_scc1 .Lcbh_done
	s_ashr_i32 s3, s28, 2
	s_and_b32 s4, s28, 3
	s_mul_i32 s35, s3, 0x42000
	s_add_u32 s32, s8, s35
	s_addc_u32 s33, s9, 0
	s_add_u32 s32, s32, 0x27e31000
	s_addc_u32 s33, s33, 0
	s_add_u32 s32, s32, s24
	s_addc_u32 s33, s33, 0
	s_mul_i32 s35, s3, 0x84000
	s_lshl_b32 s4, s4, 6
	s_add_u32 s35, s35, s4
	s_add_u32 s34, s8, s35
	s_addc_u32 s35, s9, 0
	s_add_u32 s34, s34, 0x28eb1000
	s_addc_u32 s35, s35, 0
	s_add_u32 s34, s34, s25
	s_addc_u32 s35, s35, 0
	s_mov_b32 s3, s29
.Lcbh_step:
	global_load_dwordx4 v[2:5], v9, s[32:33]
	global_load_dwordx4 v[2:5], v9, s[32:33] offset:1024
	global_load_dwordx4 v[2:5], v9, s[32:33] offset:2048
	global_load_dwordx4 v[2:5], v9, s[32:33] offset:3072
	global_load_dwordx4 v[2:5], v10, s[32:33]
	global_load_dwordx4 v[2:5], v10, s[32:33] offset:1024
	global_load_dwordx4 v[2:5], v10, s[32:33] offset:2048
	global_load_dwordx4 v[2:5], v10, s[32:33] offset:3072
	global_load_dwordx4 v[2:5], v11, s[34:35]
	global_load_dwordx4 v[2:5], v12, s[34:35]
	global_load_dwordx4 v[2:5], v13, s[34:35]
	global_load_dwordx4 v[2:5], v50, s[34:35]
	s_add_u32 s32, s32, s36
	s_addc_u32 s33, s33, 0
	s_add_u32 s34, s34, s37
	s_addc_u32 s35, s35, 0
	s_waitcnt vmcnt(48)
	s_sub_i32 s3, s3, 1
	s_cmp_lg_u32 s3, 0
	s_cbranch_scc1 .Lcbh_step
	s_add_i32 s28, s28, s0
	s_branch .Lcbh_unit
